# MoE SwiGLU epilogue rewritten by hand: packed f32 add/mul, staged over 4 element pairs, biases read from preloaded registers, store offsets via soffset
# speedup vs baseline: 1.0049x; 1.0049x over previous
.LBB0_2074:
	s_mov_b32 s32, 1
	v_lshl_or_b32 v0, s60, 7, v178
	s_mov_b32 s13, 0xc0e00000
	v_lshlrev_b32_e32 v0, 1, v0
	v_lshl_add_u32 v0, v162, 11, v0
	v_readlane_b32 s40, v252, 29
	v_readlane_b32 s41, v252, 30
	v_readlane_b32 s42, v252, 31
	v_readlane_b32 s43, v252, 32
	s_mov_b32 s50, s10
	s_mov_b32 s88, 0xbfd9db23
	s_mov_b32 s90, 0x3fb8aa3b
	v_pk_add_f32 v[130:131], v[130:131], v[34:35]
	v_pk_add_f32 v[132:133], v[132:133], v[36:37]
	v_pk_add_f32 v[126:127], v[126:127], v[206:207]
	v_pk_add_f32 v[128:129], v[128:129], v[208:209]
	v_pk_add_f32 v[98:99], v[98:99], v[212:213]
	v_pk_add_f32 v[100:101], v[100:101], v[214:215]
	v_pk_add_f32 v[94:95], v[94:95], v[216:217]
	v_pk_add_f32 v[96:97], v[96:97], v[204:205]
	v_min_f32_e32 v130, 0x40e00000, v130
	v_min_f32_e32 v131, 0x40e00000, v131
	v_min_f32_e32 v132, 0x40e00000, v132
	v_min_f32_e32 v133, 0x40e00000, v133
	v_min_f32_e32 v126, 0x40e00000, v126
	v_min_f32_e32 v127, 0x40e00000, v127
	v_min_f32_e32 v128, 0x40e00000, v128
	v_min_f32_e32 v129, 0x40e00000, v129
	v_pk_mul_f32 v[134:135], v[130:131], s[88:89] op_sel_hi:[1,0]
	v_pk_mul_f32 v[136:137], v[132:133], s[88:89] op_sel_hi:[1,0]
	v_pk_mul_f32 v[138:139], v[126:127], s[88:89] op_sel_hi:[1,0]
	v_pk_mul_f32 v[140:141], v[128:129], s[88:89] op_sel_hi:[1,0]
	v_pk_mul_f32 v[134:135], v[134:135], s[90:91] op_sel_hi:[1,0]
	v_pk_mul_f32 v[136:137], v[136:137], s[90:91] op_sel_hi:[1,0]
	v_pk_mul_f32 v[138:139], v[138:139], s[90:91] op_sel_hi:[1,0]
	v_pk_mul_f32 v[140:141], v[140:141], s[90:91] op_sel_hi:[1,0]
	v_exp_f32_e32 v134, v134
	v_exp_f32_e32 v135, v135
	v_exp_f32_e32 v136, v136
	v_exp_f32_e32 v137, v137
	v_exp_f32_e32 v138, v138
	v_exp_f32_e32 v139, v139
	v_exp_f32_e32 v140, v140
	v_exp_f32_e32 v141, v141
	v_med3_f32 v98, v98, s13, v222
	v_med3_f32 v99, v99, s13, v222
	v_med3_f32 v100, v100, s13, v222
	v_med3_f32 v101, v101, s13, v222
	v_med3_f32 v94, v94, s13, v222
	v_med3_f32 v95, v95, s13, v222
	v_med3_f32 v96, v96, s13, v222
	v_med3_f32 v97, v97, s13, v222
	v_pk_add_f32 v[134:135], v[134:135], 1.0 op_sel_hi:[1,0]
	v_pk_add_f32 v[136:137], v[136:137], 1.0 op_sel_hi:[1,0]
	v_pk_add_f32 v[138:139], v[138:139], 1.0 op_sel_hi:[1,0]
	v_pk_add_f32 v[140:141], v[140:141], 1.0 op_sel_hi:[1,0]
	v_rcp_f32_e32 v134, v134
	v_rcp_f32_e32 v135, v135
	v_rcp_f32_e32 v136, v136
	v_rcp_f32_e32 v137, v137
	v_rcp_f32_e32 v138, v138
	v_rcp_f32_e32 v139, v139
	v_rcp_f32_e32 v140, v140
	v_rcp_f32_e32 v141, v141
	v_pk_add_f32 v[98:99], v[98:99], 1.0 op_sel_hi:[1,0]
	v_pk_add_f32 v[100:101], v[100:101], 1.0 op_sel_hi:[1,0]
	v_pk_add_f32 v[94:95], v[94:95], 1.0 op_sel_hi:[1,0]
	v_pk_add_f32 v[96:97], v[96:97], 1.0 op_sel_hi:[1,0]
	v_pk_mul_f32 v[130:131], v[130:131], v[134:135]
	v_pk_mul_f32 v[132:133], v[132:133], v[136:137]
	v_pk_mul_f32 v[126:127], v[126:127], v[138:139]
	v_pk_mul_f32 v[128:129], v[128:129], v[140:141]
	v_pk_mul_f32 v[130:131], v[98:99], v[130:131]
	v_pk_mul_f32 v[132:133], v[100:101], v[132:133]
	v_pk_mul_f32 v[126:127], v[94:95], v[126:127]
	v_pk_mul_f32 v[128:129], v[96:97], v[128:129]
	v_cvt_pk_bf16_f32 v130, v130, v131
	v_cvt_pk_bf16_f32 v131, v132, v133
	v_cvt_pk_bf16_f32 v132, v126, v127
	v_cvt_pk_bf16_f32 v133, v128, v129
	buffer_store_dwordx4 v[130:133], v0, s[40:43], 0 offen sc1
	v_pk_add_f32 v[122:123], v[122:123], v[34:35]
	v_pk_add_f32 v[124:125], v[124:125], v[36:37]
	v_pk_add_f32 v[118:119], v[118:119], v[206:207]
	v_pk_add_f32 v[120:121], v[120:121], v[208:209]
	v_pk_add_f32 v[90:91], v[90:91], v[212:213]
	v_pk_add_f32 v[92:93], v[92:93], v[214:215]
	v_pk_add_f32 v[86:87], v[86:87], v[216:217]
	v_pk_add_f32 v[88:89], v[88:89], v[204:205]
	v_min_f32_e32 v122, 0x40e00000, v122
	v_min_f32_e32 v123, 0x40e00000, v123
	v_min_f32_e32 v124, 0x40e00000, v124
	v_min_f32_e32 v125, 0x40e00000, v125
	v_min_f32_e32 v118, 0x40e00000, v118
	v_min_f32_e32 v119, 0x40e00000, v119
	v_min_f32_e32 v120, 0x40e00000, v120
	v_min_f32_e32 v121, 0x40e00000, v121
	v_pk_mul_f32 v[142:143], v[122:123], s[88:89] op_sel_hi:[1,0]
	v_pk_mul_f32 v[144:145], v[124:125], s[88:89] op_sel_hi:[1,0]
	v_pk_mul_f32 v[146:147], v[118:119], s[88:89] op_sel_hi:[1,0]
	v_pk_mul_f32 v[148:149], v[120:121], s[88:89] op_sel_hi:[1,0]
	v_pk_mul_f32 v[142:143], v[142:143], s[90:91] op_sel_hi:[1,0]
	v_pk_mul_f32 v[144:145], v[144:145], s[90:91] op_sel_hi:[1,0]
	v_pk_mul_f32 v[146:147], v[146:147], s[90:91] op_sel_hi:[1,0]
	v_pk_mul_f32 v[148:149], v[148:149], s[90:91] op_sel_hi:[1,0]
	v_exp_f32_e32 v142, v142
	v_exp_f32_e32 v143, v143
	v_exp_f32_e32 v144, v144
	v_exp_f32_e32 v145, v145
	v_exp_f32_e32 v146, v146
	v_exp_f32_e32 v147, v147
	v_exp_f32_e32 v148, v148
	v_exp_f32_e32 v149, v149
	v_med3_f32 v90, v90, s13, v222
	v_med3_f32 v91, v91, s13, v222
	v_med3_f32 v92, v92, s13, v222
	v_med3_f32 v93, v93, s13, v222
	v_med3_f32 v86, v86, s13, v222
	v_med3_f32 v87, v87, s13, v222
	v_med3_f32 v88, v88, s13, v222
	v_med3_f32 v89, v89, s13, v222
	v_pk_add_f32 v[142:143], v[142:143], 1.0 op_sel_hi:[1,0]
	v_pk_add_f32 v[144:145], v[144:145], 1.0 op_sel_hi:[1,0]
	v_pk_add_f32 v[146:147], v[146:147], 1.0 op_sel_hi:[1,0]
	v_pk_add_f32 v[148:149], v[148:149], 1.0 op_sel_hi:[1,0]
	v_rcp_f32_e32 v142, v142
	v_rcp_f32_e32 v143, v143
	v_rcp_f32_e32 v144, v144
	v_rcp_f32_e32 v145, v145
	v_rcp_f32_e32 v146, v146
	v_rcp_f32_e32 v147, v147
	v_rcp_f32_e32 v148, v148
	v_rcp_f32_e32 v149, v149
	v_pk_add_f32 v[90:91], v[90:91], 1.0 op_sel_hi:[1,0]
	v_pk_add_f32 v[92:93], v[92:93], 1.0 op_sel_hi:[1,0]
	v_pk_add_f32 v[86:87], v[86:87], 1.0 op_sel_hi:[1,0]
	v_pk_add_f32 v[88:89], v[88:89], 1.0 op_sel_hi:[1,0]
	v_pk_mul_f32 v[122:123], v[122:123], v[142:143]
	v_pk_mul_f32 v[124:125], v[124:125], v[144:145]
	v_pk_mul_f32 v[118:119], v[118:119], v[146:147]
	v_pk_mul_f32 v[120:121], v[120:121], v[148:149]
	v_pk_mul_f32 v[122:123], v[90:91], v[122:123]
	v_pk_mul_f32 v[124:125], v[92:93], v[124:125]
	v_pk_mul_f32 v[118:119], v[86:87], v[118:119]
	v_pk_mul_f32 v[120:121], v[88:89], v[120:121]
	v_cvt_pk_bf16_f32 v122, v122, v123
	v_cvt_pk_bf16_f32 v123, v124, v125
	v_cvt_pk_bf16_f32 v124, v118, v119
	v_cvt_pk_bf16_f32 v125, v120, v121
	s_mov_b32 s89, 0x8000
	buffer_store_dwordx4 v[122:125], v0, s[40:43], s89 offen sc1
	v_pk_add_f32 v[114:115], v[114:115], v[34:35]
	v_pk_add_f32 v[116:117], v[116:117], v[36:37]
	v_pk_add_f32 v[110:111], v[110:111], v[206:207]
	v_pk_add_f32 v[112:113], v[112:113], v[208:209]
	v_pk_add_f32 v[82:83], v[82:83], v[212:213]
	v_pk_add_f32 v[84:85], v[84:85], v[214:215]
	v_pk_add_f32 v[78:79], v[78:79], v[216:217]
	v_pk_add_f32 v[80:81], v[80:81], v[204:205]
	v_min_f32_e32 v114, 0x40e00000, v114
	v_min_f32_e32 v115, 0x40e00000, v115
	v_min_f32_e32 v116, 0x40e00000, v116
	v_min_f32_e32 v117, 0x40e00000, v117
	v_min_f32_e32 v110, 0x40e00000, v110
	v_min_f32_e32 v111, 0x40e00000, v111
	v_min_f32_e32 v112, 0x40e00000, v112
	v_min_f32_e32 v113, 0x40e00000, v113
	v_pk_mul_f32 v[134:135], v[114:115], s[88:89] op_sel_hi:[1,0]
	v_pk_mul_f32 v[136:137], v[116:117], s[88:89] op_sel_hi:[1,0]
	v_pk_mul_f32 v[138:139], v[110:111], s[88:89] op_sel_hi:[1,0]
	v_pk_mul_f32 v[140:141], v[112:113], s[88:89] op_sel_hi:[1,0]
	v_pk_mul_f32 v[134:135], v[134:135], s[90:91] op_sel_hi:[1,0]
	v_pk_mul_f32 v[136:137], v[136:137], s[90:91] op_sel_hi:[1,0]
	v_pk_mul_f32 v[138:139], v[138:139], s[90:91] op_sel_hi:[1,0]
	v_pk_mul_f32 v[140:141], v[140:141], s[90:91] op_sel_hi:[1,0]
	v_exp_f32_e32 v134, v134
	v_exp_f32_e32 v135, v135
	v_exp_f32_e32 v136, v136
	v_exp_f32_e32 v137, v137
	v_exp_f32_e32 v138, v138
	v_exp_f32_e32 v139, v139
	v_exp_f32_e32 v140, v140
	v_exp_f32_e32 v141, v141
	v_med3_f32 v82, v82, s13, v222
	v_med3_f32 v83, v83, s13, v222
	v_med3_f32 v84, v84, s13, v222
	v_med3_f32 v85, v85, s13, v222
	v_med3_f32 v78, v78, s13, v222
	v_med3_f32 v79, v79, s13, v222
	v_med3_f32 v80, v80, s13, v222
	v_med3_f32 v81, v81, s13, v222
	v_pk_add_f32 v[134:135], v[134:135], 1.0 op_sel_hi:[1,0]
	v_pk_add_f32 v[136:137], v[136:137], 1.0 op_sel_hi:[1,0]
	v_pk_add_f32 v[138:139], v[138:139], 1.0 op_sel_hi:[1,0]
	v_pk_add_f32 v[140:141], v[140:141], 1.0 op_sel_hi:[1,0]
	v_rcp_f32_e32 v134, v134
	v_rcp_f32_e32 v135, v135
	v_rcp_f32_e32 v136, v136
	v_rcp_f32_e32 v137, v137
	v_rcp_f32_e32 v138, v138
	v_rcp_f32_e32 v139, v139
	v_rcp_f32_e32 v140, v140
	v_rcp_f32_e32 v141, v141
	v_pk_add_f32 v[82:83], v[82:83], 1.0 op_sel_hi:[1,0]
	v_pk_add_f32 v[84:85], v[84:85], 1.0 op_sel_hi:[1,0]
	v_pk_add_f32 v[78:79], v[78:79], 1.0 op_sel_hi:[1,0]
	v_pk_add_f32 v[80:81], v[80:81], 1.0 op_sel_hi:[1,0]
	v_pk_mul_f32 v[114:115], v[114:115], v[134:135]
	v_pk_mul_f32 v[116:117], v[116:117], v[136:137]
	v_pk_mul_f32 v[110:111], v[110:111], v[138:139]
	v_pk_mul_f32 v[112:113], v[112:113], v[140:141]
	v_pk_mul_f32 v[114:115], v[82:83], v[114:115]
	v_pk_mul_f32 v[116:117], v[84:85], v[116:117]
	v_pk_mul_f32 v[110:111], v[78:79], v[110:111]
	v_pk_mul_f32 v[112:113], v[80:81], v[112:113]
	v_cvt_pk_bf16_f32 v114, v114, v115
	v_cvt_pk_bf16_f32 v115, v116, v117
	v_cvt_pk_bf16_f32 v116, v110, v111
	v_cvt_pk_bf16_f32 v117, v112, v113
	s_mov_b32 s89, 0x10000
	buffer_store_dwordx4 v[114:117], v0, s[40:43], s89 offen sc1
	v_pk_add_f32 v[106:107], v[106:107], v[34:35]
	v_pk_add_f32 v[108:109], v[108:109], v[36:37]
	v_pk_add_f32 v[102:103], v[102:103], v[206:207]
	v_pk_add_f32 v[104:105], v[104:105], v[208:209]
	v_pk_add_f32 v[74:75], v[74:75], v[212:213]
	v_pk_add_f32 v[76:77], v[76:77], v[214:215]
	v_pk_add_f32 v[70:71], v[70:71], v[216:217]
	v_pk_add_f32 v[72:73], v[72:73], v[204:205]
	v_min_f32_e32 v106, 0x40e00000, v106
	v_min_f32_e32 v107, 0x40e00000, v107
	v_min_f32_e32 v108, 0x40e00000, v108
	v_min_f32_e32 v109, 0x40e00000, v109
	v_min_f32_e32 v102, 0x40e00000, v102
	v_min_f32_e32 v103, 0x40e00000, v103
	v_min_f32_e32 v104, 0x40e00000, v104
	v_min_f32_e32 v105, 0x40e00000, v105
	v_pk_mul_f32 v[142:143], v[106:107], s[88:89] op_sel_hi:[1,0]
	v_pk_mul_f32 v[144:145], v[108:109], s[88:89] op_sel_hi:[1,0]
	v_pk_mul_f32 v[146:147], v[102:103], s[88:89] op_sel_hi:[1,0]
	v_pk_mul_f32 v[148:149], v[104:105], s[88:89] op_sel_hi:[1,0]
	v_pk_mul_f32 v[142:143], v[142:143], s[90:91] op_sel_hi:[1,0]
	v_pk_mul_f32 v[144:145], v[144:145], s[90:91] op_sel_hi:[1,0]
	v_pk_mul_f32 v[146:147], v[146:147], s[90:91] op_sel_hi:[1,0]
	v_pk_mul_f32 v[148:149], v[148:149], s[90:91] op_sel_hi:[1,0]
	v_exp_f32_e32 v142, v142
	v_exp_f32_e32 v143, v143
	v_exp_f32_e32 v144, v144
	v_exp_f32_e32 v145, v145
	v_exp_f32_e32 v146, v146
	v_exp_f32_e32 v147, v147
	v_exp_f32_e32 v148, v148
	v_exp_f32_e32 v149, v149
	v_med3_f32 v74, v74, s13, v222
	v_med3_f32 v75, v75, s13, v222
	v_med3_f32 v76, v76, s13, v222
	v_med3_f32 v77, v77, s13, v222
	v_med3_f32 v70, v70, s13, v222
	v_med3_f32 v71, v71, s13, v222
	v_med3_f32 v72, v72, s13, v222
	v_med3_f32 v73, v73, s13, v222
	v_pk_add_f32 v[142:143], v[142:143], 1.0 op_sel_hi:[1,0]
	v_pk_add_f32 v[144:145], v[144:145], 1.0 op_sel_hi:[1,0]
	v_pk_add_f32 v[146:147], v[146:147], 1.0 op_sel_hi:[1,0]
	v_pk_add_f32 v[148:149], v[148:149], 1.0 op_sel_hi:[1,0]
	v_rcp_f32_e32 v142, v142
	v_rcp_f32_e32 v143, v143
	v_rcp_f32_e32 v144, v144
	v_rcp_f32_e32 v145, v145
	v_rcp_f32_e32 v146, v146
	v_rcp_f32_e32 v147, v147
	v_rcp_f32_e32 v148, v148
	v_rcp_f32_e32 v149, v149
	v_pk_add_f32 v[74:75], v[74:75], 1.0 op_sel_hi:[1,0]
	v_pk_add_f32 v[76:77], v[76:77], 1.0 op_sel_hi:[1,0]
	v_pk_add_f32 v[70:71], v[70:71], 1.0 op_sel_hi:[1,0]
	v_pk_add_f32 v[72:73], v[72:73], 1.0 op_sel_hi:[1,0]
	v_pk_mul_f32 v[106:107], v[106:107], v[142:143]
	v_pk_mul_f32 v[108:109], v[108:109], v[144:145]
	v_pk_mul_f32 v[102:103], v[102:103], v[146:147]
	v_pk_mul_f32 v[104:105], v[104:105], v[148:149]
	v_pk_mul_f32 v[106:107], v[74:75], v[106:107]
	v_pk_mul_f32 v[108:109], v[76:77], v[108:109]
	v_pk_mul_f32 v[102:103], v[70:71], v[102:103]
	v_pk_mul_f32 v[104:105], v[72:73], v[104:105]
	v_cvt_pk_bf16_f32 v106, v106, v107
	v_cvt_pk_bf16_f32 v107, v108, v109
	v_cvt_pk_bf16_f32 v108, v102, v103
	v_cvt_pk_bf16_f32 v109, v104, v105
	s_mov_b32 s89, 0x18000
	buffer_store_dwordx4 v[106:109], v0, s[40:43], s89 offen sc1
	v_pk_add_f32 v[66:67], v[66:67], v[34:35]
	v_pk_add_f32 v[68:69], v[68:69], v[36:37]
	v_pk_add_f32 v[62:63], v[62:63], v[206:207]
	v_pk_add_f32 v[64:65], v[64:65], v[208:209]
	v_pk_add_f32 v[30:31], v[30:31], v[212:213]
	v_pk_add_f32 v[32:33], v[32:33], v[214:215]
	v_pk_add_f32 v[26:27], v[26:27], v[216:217]
	v_pk_add_f32 v[28:29], v[28:29], v[204:205]
	v_min_f32_e32 v66, 0x40e00000, v66
	v_min_f32_e32 v67, 0x40e00000, v67
	v_min_f32_e32 v68, 0x40e00000, v68
	v_min_f32_e32 v69, 0x40e00000, v69
	v_min_f32_e32 v62, 0x40e00000, v62
	v_min_f32_e32 v63, 0x40e00000, v63
	v_min_f32_e32 v64, 0x40e00000, v64
	v_min_f32_e32 v65, 0x40e00000, v65
	v_pk_mul_f32 v[134:135], v[66:67], s[88:89] op_sel_hi:[1,0]
	v_pk_mul_f32 v[136:137], v[68:69], s[88:89] op_sel_hi:[1,0]
	v_pk_mul_f32 v[138:139], v[62:63], s[88:89] op_sel_hi:[1,0]
	v_pk_mul_f32 v[140:141], v[64:65], s[88:89] op_sel_hi:[1,0]
	v_pk_mul_f32 v[134:135], v[134:135], s[90:91] op_sel_hi:[1,0]
	v_pk_mul_f32 v[136:137], v[136:137], s[90:91] op_sel_hi:[1,0]
	v_pk_mul_f32 v[138:139], v[138:139], s[90:91] op_sel_hi:[1,0]
	v_pk_mul_f32 v[140:141], v[140:141], s[90:91] op_sel_hi:[1,0]
	v_exp_f32_e32 v134, v134
	v_exp_f32_e32 v135, v135
	v_exp_f32_e32 v136, v136
	v_exp_f32_e32 v137, v137
	v_exp_f32_e32 v138, v138
	v_exp_f32_e32 v139, v139
	v_exp_f32_e32 v140, v140
	v_exp_f32_e32 v141, v141
	v_med3_f32 v30, v30, s13, v222
	v_med3_f32 v31, v31, s13, v222
	v_med3_f32 v32, v32, s13, v222
	v_med3_f32 v33, v33, s13, v222
	v_med3_f32 v26, v26, s13, v222
	v_med3_f32 v27, v27, s13, v222
	v_med3_f32 v28, v28, s13, v222
	v_med3_f32 v29, v29, s13, v222
	v_pk_add_f32 v[134:135], v[134:135], 1.0 op_sel_hi:[1,0]
	v_pk_add_f32 v[136:137], v[136:137], 1.0 op_sel_hi:[1,0]
	v_pk_add_f32 v[138:139], v[138:139], 1.0 op_sel_hi:[1,0]
	v_pk_add_f32 v[140:141], v[140:141], 1.0 op_sel_hi:[1,0]
	v_rcp_f32_e32 v134, v134
	v_rcp_f32_e32 v135, v135
	v_rcp_f32_e32 v136, v136
	v_rcp_f32_e32 v137, v137
	v_rcp_f32_e32 v138, v138
	v_rcp_f32_e32 v139, v139
	v_rcp_f32_e32 v140, v140
	v_rcp_f32_e32 v141, v141
	v_pk_add_f32 v[30:31], v[30:31], 1.0 op_sel_hi:[1,0]
	v_pk_add_f32 v[32:33], v[32:33], 1.0 op_sel_hi:[1,0]
	v_pk_add_f32 v[26:27], v[26:27], 1.0 op_sel_hi:[1,0]
	v_pk_add_f32 v[28:29], v[28:29], 1.0 op_sel_hi:[1,0]
	v_pk_mul_f32 v[66:67], v[66:67], v[134:135]
	v_pk_mul_f32 v[68:69], v[68:69], v[136:137]
	v_pk_mul_f32 v[62:63], v[62:63], v[138:139]
	v_pk_mul_f32 v[64:65], v[64:65], v[140:141]
	v_pk_mul_f32 v[66:67], v[30:31], v[66:67]
	v_pk_mul_f32 v[68:69], v[32:33], v[68:69]
	v_pk_mul_f32 v[62:63], v[26:27], v[62:63]
	v_pk_mul_f32 v[64:65], v[28:29], v[64:65]
	v_cvt_pk_bf16_f32 v66, v66, v67
	v_cvt_pk_bf16_f32 v67, v68, v69
	v_cvt_pk_bf16_f32 v68, v62, v63
	v_cvt_pk_bf16_f32 v69, v64, v65
	s_mov_b32 s89, 0x40000
	buffer_store_dwordx4 v[66:69], v0, s[40:43], s89 offen sc1
	v_pk_add_f32 v[58:59], v[58:59], v[34:35]
	v_pk_add_f32 v[60:61], v[60:61], v[36:37]
	v_pk_add_f32 v[54:55], v[54:55], v[206:207]
	v_pk_add_f32 v[56:57], v[56:57], v[208:209]
	v_pk_add_f32 v[22:23], v[22:23], v[212:213]
	v_pk_add_f32 v[24:25], v[24:25], v[214:215]
	v_pk_add_f32 v[18:19], v[18:19], v[216:217]
	v_pk_add_f32 v[20:21], v[20:21], v[204:205]
	v_min_f32_e32 v58, 0x40e00000, v58
	v_min_f32_e32 v59, 0x40e00000, v59
	v_min_f32_e32 v60, 0x40e00000, v60
	v_min_f32_e32 v61, 0x40e00000, v61
	v_min_f32_e32 v54, 0x40e00000, v54
	v_min_f32_e32 v55, 0x40e00000, v55
	v_min_f32_e32 v56, 0x40e00000, v56
	v_min_f32_e32 v57, 0x40e00000, v57
	v_pk_mul_f32 v[142:143], v[58:59], s[88:89] op_sel_hi:[1,0]
	v_pk_mul_f32 v[144:145], v[60:61], s[88:89] op_sel_hi:[1,0]
	v_pk_mul_f32 v[146:147], v[54:55], s[88:89] op_sel_hi:[1,0]
	v_pk_mul_f32 v[148:149], v[56:57], s[88:89] op_sel_hi:[1,0]
	v_pk_mul_f32 v[142:143], v[142:143], s[90:91] op_sel_hi:[1,0]
	v_pk_mul_f32 v[144:145], v[144:145], s[90:91] op_sel_hi:[1,0]
	v_pk_mul_f32 v[146:147], v[146:147], s[90:91] op_sel_hi:[1,0]
	v_pk_mul_f32 v[148:149], v[148:149], s[90:91] op_sel_hi:[1,0]
	v_exp_f32_e32 v142, v142
	v_exp_f32_e32 v143, v143
	v_exp_f32_e32 v144, v144
	v_exp_f32_e32 v145, v145
	v_exp_f32_e32 v146, v146
	v_exp_f32_e32 v147, v147
	v_exp_f32_e32 v148, v148
	v_exp_f32_e32 v149, v149
	v_med3_f32 v22, v22, s13, v222
	v_med3_f32 v23, v23, s13, v222
	v_med3_f32 v24, v24, s13, v222
	v_med3_f32 v25, v25, s13, v222
	v_med3_f32 v18, v18, s13, v222
	v_med3_f32 v19, v19, s13, v222
	v_med3_f32 v20, v20, s13, v222
	v_med3_f32 v21, v21, s13, v222
	v_pk_add_f32 v[142:143], v[142:143], 1.0 op_sel_hi:[1,0]
	v_pk_add_f32 v[144:145], v[144:145], 1.0 op_sel_hi:[1,0]
	v_pk_add_f32 v[146:147], v[146:147], 1.0 op_sel_hi:[1,0]
	v_pk_add_f32 v[148:149], v[148:149], 1.0 op_sel_hi:[1,0]
	v_rcp_f32_e32 v142, v142
	v_rcp_f32_e32 v143, v143
	v_rcp_f32_e32 v144, v144
	v_rcp_f32_e32 v145, v145
	v_rcp_f32_e32 v146, v146
	v_rcp_f32_e32 v147, v147
	v_rcp_f32_e32 v148, v148
	v_rcp_f32_e32 v149, v149
	v_pk_add_f32 v[22:23], v[22:23], 1.0 op_sel_hi:[1,0]
	v_pk_add_f32 v[24:25], v[24:25], 1.0 op_sel_hi:[1,0]
	v_pk_add_f32 v[18:19], v[18:19], 1.0 op_sel_hi:[1,0]
	v_pk_add_f32 v[20:21], v[20:21], 1.0 op_sel_hi:[1,0]
	v_pk_mul_f32 v[58:59], v[58:59], v[142:143]
	v_pk_mul_f32 v[60:61], v[60:61], v[144:145]
	v_pk_mul_f32 v[54:55], v[54:55], v[146:147]
	v_pk_mul_f32 v[56:57], v[56:57], v[148:149]
	v_pk_mul_f32 v[58:59], v[22:23], v[58:59]
	v_pk_mul_f32 v[60:61], v[24:25], v[60:61]
	v_pk_mul_f32 v[54:55], v[18:19], v[54:55]
	v_pk_mul_f32 v[56:57], v[20:21], v[56:57]
	v_cvt_pk_bf16_f32 v58, v58, v59
	v_cvt_pk_bf16_f32 v59, v60, v61
	v_cvt_pk_bf16_f32 v60, v54, v55
	v_cvt_pk_bf16_f32 v61, v56, v57
	s_mov_b32 s89, 0x48000
	buffer_store_dwordx4 v[58:61], v0, s[40:43], s89 offen sc1
	v_pk_add_f32 v[50:51], v[50:51], v[34:35]
	v_pk_add_f32 v[52:53], v[52:53], v[36:37]
	v_pk_add_f32 v[46:47], v[46:47], v[206:207]
	v_pk_add_f32 v[48:49], v[48:49], v[208:209]
	v_pk_add_f32 v[14:15], v[14:15], v[212:213]
	v_pk_add_f32 v[16:17], v[16:17], v[214:215]
	v_pk_add_f32 v[10:11], v[10:11], v[216:217]
	v_pk_add_f32 v[12:13], v[12:13], v[204:205]
	v_min_f32_e32 v50, 0x40e00000, v50
	v_min_f32_e32 v51, 0x40e00000, v51
	v_min_f32_e32 v52, 0x40e00000, v52
	v_min_f32_e32 v53, 0x40e00000, v53
	v_min_f32_e32 v46, 0x40e00000, v46
	v_min_f32_e32 v47, 0x40e00000, v47
	v_min_f32_e32 v48, 0x40e00000, v48
	v_min_f32_e32 v49, 0x40e00000, v49
	v_pk_mul_f32 v[134:135], v[50:51], s[88:89] op_sel_hi:[1,0]
	v_pk_mul_f32 v[136:137], v[52:53], s[88:89] op_sel_hi:[1,0]
	v_pk_mul_f32 v[138:139], v[46:47], s[88:89] op_sel_hi:[1,0]
	v_pk_mul_f32 v[140:141], v[48:49], s[88:89] op_sel_hi:[1,0]
	v_pk_mul_f32 v[134:135], v[134:135], s[90:91] op_sel_hi:[1,0]
	v_pk_mul_f32 v[136:137], v[136:137], s[90:91] op_sel_hi:[1,0]
	v_pk_mul_f32 v[138:139], v[138:139], s[90:91] op_sel_hi:[1,0]
	v_pk_mul_f32 v[140:141], v[140:141], s[90:91] op_sel_hi:[1,0]
	v_exp_f32_e32 v134, v134
	v_exp_f32_e32 v135, v135
	v_exp_f32_e32 v136, v136
	v_exp_f32_e32 v137, v137
	v_exp_f32_e32 v138, v138
	v_exp_f32_e32 v139, v139
	v_exp_f32_e32 v140, v140
	v_exp_f32_e32 v141, v141
	v_med3_f32 v14, v14, s13, v222
	v_med3_f32 v15, v15, s13, v222
	v_med3_f32 v16, v16, s13, v222
	v_med3_f32 v17, v17, s13, v222
	v_med3_f32 v10, v10, s13, v222
	v_med3_f32 v11, v11, s13, v222
	v_med3_f32 v12, v12, s13, v222
	v_med3_f32 v13, v13, s13, v222
	v_pk_add_f32 v[134:135], v[134:135], 1.0 op_sel_hi:[1,0]
	v_pk_add_f32 v[136:137], v[136:137], 1.0 op_sel_hi:[1,0]
	v_pk_add_f32 v[138:139], v[138:139], 1.0 op_sel_hi:[1,0]
	v_pk_add_f32 v[140:141], v[140:141], 1.0 op_sel_hi:[1,0]
	v_rcp_f32_e32 v134, v134
	v_rcp_f32_e32 v135, v135
	v_rcp_f32_e32 v136, v136
	v_rcp_f32_e32 v137, v137
	v_rcp_f32_e32 v138, v138
	v_rcp_f32_e32 v139, v139
	v_rcp_f32_e32 v140, v140
	v_rcp_f32_e32 v141, v141
	v_pk_add_f32 v[14:15], v[14:15], 1.0 op_sel_hi:[1,0]
	v_pk_add_f32 v[16:17], v[16:17], 1.0 op_sel_hi:[1,0]
	v_pk_add_f32 v[10:11], v[10:11], 1.0 op_sel_hi:[1,0]
	v_pk_add_f32 v[12:13], v[12:13], 1.0 op_sel_hi:[1,0]
	v_pk_mul_f32 v[50:51], v[50:51], v[134:135]
	v_pk_mul_f32 v[52:53], v[52:53], v[136:137]
	v_pk_mul_f32 v[46:47], v[46:47], v[138:139]
	v_pk_mul_f32 v[48:49], v[48:49], v[140:141]
	v_pk_mul_f32 v[50:51], v[14:15], v[50:51]
	v_pk_mul_f32 v[52:53], v[16:17], v[52:53]
	v_pk_mul_f32 v[46:47], v[10:11], v[46:47]
	v_pk_mul_f32 v[48:49], v[12:13], v[48:49]
	v_cvt_pk_bf16_f32 v50, v50, v51
	v_cvt_pk_bf16_f32 v51, v52, v53
	v_cvt_pk_bf16_f32 v52, v46, v47
	v_cvt_pk_bf16_f32 v53, v48, v49
	s_mov_b32 s89, 0x50000
	buffer_store_dwordx4 v[50:53], v0, s[40:43], s89 offen sc1
	v_pk_add_f32 v[42:43], v[42:43], v[34:35]
	v_pk_add_f32 v[44:45], v[44:45], v[36:37]
	v_pk_add_f32 v[38:39], v[38:39], v[206:207]
	v_pk_add_f32 v[40:41], v[40:41], v[208:209]
	v_pk_add_f32 v[6:7], v[6:7], v[212:213]
	v_pk_add_f32 v[8:9], v[8:9], v[214:215]
	v_pk_add_f32 v[2:3], v[2:3], v[216:217]
	v_pk_add_f32 v[4:5], v[4:5], v[204:205]
	v_min_f32_e32 v42, 0x40e00000, v42
	v_min_f32_e32 v43, 0x40e00000, v43
	v_min_f32_e32 v44, 0x40e00000, v44
	v_min_f32_e32 v45, 0x40e00000, v45
	v_min_f32_e32 v38, 0x40e00000, v38
	v_min_f32_e32 v39, 0x40e00000, v39
	v_min_f32_e32 v40, 0x40e00000, v40
	v_min_f32_e32 v41, 0x40e00000, v41
	v_pk_mul_f32 v[142:143], v[42:43], s[88:89] op_sel_hi:[1,0]
	v_pk_mul_f32 v[144:145], v[44:45], s[88:89] op_sel_hi:[1,0]
	v_pk_mul_f32 v[146:147], v[38:39], s[88:89] op_sel_hi:[1,0]
	v_pk_mul_f32 v[148:149], v[40:41], s[88:89] op_sel_hi:[1,0]
	v_pk_mul_f32 v[142:143], v[142:143], s[90:91] op_sel_hi:[1,0]
	v_pk_mul_f32 v[144:145], v[144:145], s[90:91] op_sel_hi:[1,0]
	v_pk_mul_f32 v[146:147], v[146:147], s[90:91] op_sel_hi:[1,0]
	v_pk_mul_f32 v[148:149], v[148:149], s[90:91] op_sel_hi:[1,0]
	v_exp_f32_e32 v142, v142
	v_exp_f32_e32 v143, v143
	v_exp_f32_e32 v144, v144
	v_exp_f32_e32 v145, v145
	v_exp_f32_e32 v146, v146
	v_exp_f32_e32 v147, v147
	v_exp_f32_e32 v148, v148
	v_exp_f32_e32 v149, v149
	v_med3_f32 v6, v6, s13, v222
	v_med3_f32 v7, v7, s13, v222
	v_med3_f32 v8, v8, s13, v222
	v_med3_f32 v9, v9, s13, v222
	v_med3_f32 v2, v2, s13, v222
	v_med3_f32 v3, v3, s13, v222
	v_med3_f32 v4, v4, s13, v222
	v_med3_f32 v5, v5, s13, v222
	v_pk_add_f32 v[142:143], v[142:143], 1.0 op_sel_hi:[1,0]
	v_pk_add_f32 v[144:145], v[144:145], 1.0 op_sel_hi:[1,0]
	v_pk_add_f32 v[146:147], v[146:147], 1.0 op_sel_hi:[1,0]
	v_pk_add_f32 v[148:149], v[148:149], 1.0 op_sel_hi:[1,0]
	v_rcp_f32_e32 v142, v142
	v_rcp_f32_e32 v143, v143
	v_rcp_f32_e32 v144, v144
	v_rcp_f32_e32 v145, v145
	v_rcp_f32_e32 v146, v146
	v_rcp_f32_e32 v147, v147
	v_rcp_f32_e32 v148, v148
	v_rcp_f32_e32 v149, v149
	v_pk_add_f32 v[6:7], v[6:7], 1.0 op_sel_hi:[1,0]
	v_pk_add_f32 v[8:9], v[8:9], 1.0 op_sel_hi:[1,0]
	v_pk_add_f32 v[2:3], v[2:3], 1.0 op_sel_hi:[1,0]
	v_pk_add_f32 v[4:5], v[4:5], 1.0 op_sel_hi:[1,0]
	v_pk_mul_f32 v[42:43], v[42:43], v[142:143]
	v_pk_mul_f32 v[44:45], v[44:45], v[144:145]
	v_pk_mul_f32 v[38:39], v[38:39], v[146:147]
	v_pk_mul_f32 v[40:41], v[40:41], v[148:149]
	v_pk_mul_f32 v[42:43], v[6:7], v[42:43]
	v_pk_mul_f32 v[44:45], v[8:9], v[44:45]
	v_pk_mul_f32 v[38:39], v[2:3], v[38:39]
	v_pk_mul_f32 v[40:41], v[4:5], v[40:41]
	v_cvt_pk_bf16_f32 v42, v42, v43
	v_cvt_pk_bf16_f32 v43, v44, v45
	v_cvt_pk_bf16_f32 v44, v38, v39
	v_cvt_pk_bf16_f32 v45, v40, v41
	s_mov_b32 s89, 0x58000
	buffer_store_dwordx4 v[42:45], v0, s[40:43], s89 offen sc1
	s_waitcnt vmcnt(8)
	s_add_u32 s42, s29, 0xffffff00
	s_addc_u32 s43, s31, -1
	s_and_b64 vcc, exec, s[0:1]
	s_cbranch_vccz .LBB0_2070
